# PEER stage K: 16 LDS fragment reads feeding the score MFMAs rotate over four register quads and run three reads ahead (were read / lgkmcnt(0) / MFMA one at a time through one quad)
# speedup vs baseline: 1.0026x; 1.0004x over previous
; #define LAS __attribute__((address_space(3)))
; __device__ __forceinline__ void peer_unit(Frame& F, const Args& a, int layer, int unit, bool last) {
;     ...
;             const LAS bf16* sKc = sKey + (jp & 1) * 128 * TP;
;             f32x4 sc[8];
; #pragma unroll
;             for (int nt = 0; nt < 8; ++nt) sc[nt] = (f32x4){KOFF, KOFF, KOFF, KOFF};
; #pragma unroll
;             for (int kk = 0; kk < 4; ++kk)
; #pragma unroll
;                 for (int nt = 0; nt < 8; ++nt) { const bf16x8 kf = *(const LAS bf16x8*)(sKc + (16 * nt + fr) * TP + 32 * kk + 8 * fq);
;                     sc[nt] = __builtin_amdgcn_mfma_f32_16x16x32_bf16(kf, qf[kk], sc[nt], 0, 0, 0); }
;             unsigned t[32];
; #pragma unroll
;             for (int nt = 0; nt < 8; ++nt)
; #pragma unroll
;                 for (int rg = 0; rg < 4; ++rg) t[4 * nt + rg] = (__float_as_uint(sc[nt][rg]) & 0xFFFFFF80u) | (unsigned)(16 * nt + 4 * fq + rg);
.LBB0_1709:
	s_mul_i32 s5, s55, 0x8800
	v_add_u32_e32 v72, s5, v113
	ds_read_b128 v[64:67], v72
	ds_read_b128 v[114:117], v72 offset:4352
	ds_read_b128 v[118:121], v72 offset:8704
	ds_read_b128 v[122:125], v72 offset:13056
	ds_read_b128 v[126:129], v72 offset:17408
	ds_read_b128 v[130:133], v72 offset:21760
	ds_read_b128 v[134:137], v72 offset:26112
	ds_read_b128 v[138:141], v72 offset:30464
	s_mov_b32 s6, s4
	s_mov_b32 s7, s4
	s_mov_b32 s5, s4
	v_mov_b64_e32 v[70:71], s[6:7]
	v_mov_b64_e32 v[68:69], s[4:5]
	s_andn2_b64 vcc, exec, s[52:53]
	s_waitcnt lgkmcnt(7)
	v_mfma_f32_16x16x32_bf16 v[64:67], v[64:67], v[18:21], v[68:71]
	s_waitcnt lgkmcnt(6)
	v_mfma_f32_16x16x32_bf16 v[114:117], v[114:117], v[18:21], v[68:71]
	s_waitcnt lgkmcnt(5)
	v_mfma_f32_16x16x32_bf16 v[118:121], v[118:121], v[18:21], v[68:71]
	s_waitcnt lgkmcnt(4)
	v_mfma_f32_16x16x32_bf16 v[122:125], v[122:125], v[18:21], v[68:71]
	s_waitcnt lgkmcnt(3)
	v_mfma_f32_16x16x32_bf16 v[126:129], v[126:129], v[18:21], v[68:71]
	s_waitcnt lgkmcnt(2)
	v_mfma_f32_16x16x32_bf16 v[130:133], v[130:133], v[18:21], v[68:71]
	s_waitcnt lgkmcnt(1)
	v_mfma_f32_16x16x32_bf16 v[134:137], v[134:137], v[18:21], v[68:71]
	s_waitcnt lgkmcnt(0)
	v_mfma_f32_16x16x32_bf16 v[68:71], v[138:141], v[18:21], v[68:71]
	ds_read_b128 v[138:141], v72 offset:64
	ds_read_b128 v[156:159], v72 offset:4416
	ds_read_b128 v[160:163], v72 offset:8768
	ds_read_b128 v[164:167], v72 offset:13120
	s_waitcnt lgkmcnt(3)
	v_mfma_f32_16x16x32_bf16 v[64:67], v[138:141], v[22:25], v[64:67]
	ds_read_b128 v[138:141], v72 offset:17472
	s_waitcnt lgkmcnt(3)
	v_mfma_f32_16x16x32_bf16 v[114:117], v[156:159], v[22:25], v[114:117]
	ds_read_b128 v[156:159], v72 offset:21824
	s_waitcnt lgkmcnt(3)
	v_mfma_f32_16x16x32_bf16 v[118:121], v[160:163], v[22:25], v[118:121]
	ds_read_b128 v[160:163], v72 offset:26176
	s_waitcnt lgkmcnt(3)
	v_mfma_f32_16x16x32_bf16 v[122:125], v[164:167], v[22:25], v[122:125]
	ds_read_b128 v[164:167], v72 offset:30528
	s_waitcnt lgkmcnt(3)
	v_mfma_f32_16x16x32_bf16 v[126:129], v[138:141], v[22:25], v[126:129]
	ds_read_b128 v[138:141], v72 offset:128
	s_waitcnt lgkmcnt(3)
	v_mfma_f32_16x16x32_bf16 v[130:133], v[156:159], v[22:25], v[130:133]
	ds_read_b128 v[156:159], v72 offset:4480
	s_waitcnt lgkmcnt(3)
	v_mfma_f32_16x16x32_bf16 v[134:137], v[160:163], v[22:25], v[134:137]
	ds_read_b128 v[160:163], v72 offset:8832
	s_waitcnt lgkmcnt(3)
	v_mfma_f32_16x16x32_bf16 v[68:71], v[164:167], v[22:25], v[68:71]
	ds_read_b128 v[164:167], v72 offset:13184
	s_waitcnt lgkmcnt(3)
	v_mfma_f32_16x16x32_bf16 v[64:67], v[138:141], v[26:29], v[64:67]
	ds_read_b128 v[138:141], v72 offset:17536
	s_waitcnt lgkmcnt(3)
	v_mfma_f32_16x16x32_bf16 v[114:117], v[156:159], v[26:29], v[114:117]
	ds_read_b128 v[156:159], v72 offset:21888
	s_waitcnt lgkmcnt(3)
	v_mfma_f32_16x16x32_bf16 v[118:121], v[160:163], v[26:29], v[118:121]
	ds_read_b128 v[160:163], v72 offset:26240
	s_waitcnt lgkmcnt(3)
	v_mfma_f32_16x16x32_bf16 v[122:125], v[164:167], v[26:29], v[122:125]
	ds_read_b128 v[164:167], v72 offset:30592
	s_waitcnt lgkmcnt(3)
	v_mfma_f32_16x16x32_bf16 v[126:129], v[138:141], v[26:29], v[126:129]
	s_waitcnt lgkmcnt(2)
	v_mfma_f32_16x16x32_bf16 v[130:133], v[156:159], v[26:29], v[130:133]
	s_waitcnt lgkmcnt(1)
	v_mfma_f32_16x16x32_bf16 v[134:137], v[160:163], v[26:29], v[134:137]
	s_waitcnt lgkmcnt(0)
	v_mfma_f32_16x16x32_bf16 v[68:71], v[164:167], v[26:29], v[68:71]
	ds_read_b128 v[138:141], v72 offset:192
	s_waitcnt lgkmcnt(0)
	v_mfma_f32_16x16x32_bf16 v[64:67], v[138:141], v[30:33], v[64:67]
	ds_read_b128 v[138:141], v72 offset:4544
	s_nop 6
	v_and_or_b32 v64, v64, s85, v76
	s_waitcnt lgkmcnt(0)
	v_mfma_f32_16x16x32_bf16 v[114:117], v[138:141], v[30:33], v[114:117]
	ds_read_b128 v[138:141], v72 offset:8896
	v_and_or_b32 v65, v65, s85, v89
	v_and_or_b32 v66, v66, s85, v90
	s_waitcnt lgkmcnt(0)
	v_mfma_f32_16x16x32_bf16 v[118:121], v[138:141], v[30:33], v[118:121]
	ds_read_b128 v[138:141], v72 offset:13248
	v_and_or_b32 v67, v67, s85, v91
	s_nop 0
	v_and_or_b32 v73, v115, s85, v92
	s_waitcnt lgkmcnt(0)
	v_mfma_f32_16x16x32_bf16 v[122:125], v[138:141], v[30:33], v[122:125]
	ds_read_b128 v[138:141], v72 offset:17600
	v_and_or_b32 v115, v117, s85, v94
	v_and_or_b32 v117, v119, s85, v95
	s_waitcnt lgkmcnt(0)
	v_mfma_f32_16x16x32_bf16 v[126:129], v[138:141], v[30:33], v[126:129]
	ds_read_b128 v[138:141], v72 offset:21952
	v_and_or_b32 v119, v121, s85, v97
	s_nop 0
	v_and_or_b32 v121, v123, s85, v98
	s_waitcnt lgkmcnt(0)
	v_mfma_f32_16x16x32_bf16 v[130:133], v[138:141], v[30:33], v[130:133]
	ds_read_b128 v[138:141], v72 offset:26304
	v_and_or_b32 v123, v125, s85, v100
	v_and_or_b32 v125, v127, s85, v101
	s_waitcnt lgkmcnt(0)
	v_mfma_f32_16x16x32_bf16 v[134:137], v[138:141], v[30:33], v[134:137]
	ds_read_b128 v[138:141], v72 offset:30656
	v_and_or_b32 v72, v114, s85, v82
	v_and_or_b32 v114, v116, s85, v93
	s_waitcnt lgkmcnt(0)
; #define CE_DESC(a, b) do { const unsigned _h = max((a), (b)), _l = min((a), (b)); (a) = _h; (b) = _l; } while (0)
; template <int OFF> __device__ __forceinline__ void bitonic_sort16(unsigned (&x)[32]) {
; #pragma unroll
;     for (int k = 2; k <= 16; k <<= 1)
; #pragma unroll
;         for (int j = k >> 1; j >= 1; j >>= 1)
; #pragma unroll
;             for (int i = 0; i < 16; ++i) { const int l = i ^ j; if (l > i) { if ((i & k) == 0 || k == 16) CE_DESC(x[OFF + i], x[OFF + l]); else CE_DESC(x[OFF + l], x[OFF + i]); } }
; __device__ __forceinline__ void peer_unit(Frame& F, const Args& a, int layer, int unit, bool last) {
;     ...
;             unsigned t[32];
; #pragma unroll
;             for (int nt = 0; nt < 8; ++nt)
; #pragma unroll
;                 for (int rg = 0; rg < 4; ++rg) t[4 * nt + rg] = (__float_as_uint(sc[nt][rg]) & 0xFFFFFF80u) | (unsigned)(16 * nt + 4 * fq + rg);
;             bitonic_sort16<0>(t); bitonic_sort16<16>(t);
	v_mfma_f32_16x16x32_bf16 v[68:71], v[138:141], v[30:33], v[68:71]
	v_and_or_b32 v116, v118, s85, v83
	v_and_or_b32 v118, v120, s85, v96
	v_and_or_b32 v120, v122, s85, v84
	v_and_or_b32 v122, v124, s85, v99
	v_and_or_b32 v124, v126, s85, v85
	v_and_or_b32 v126, v128, s85, v102
	v_and_or_b32 v127, v129, s85, v103
	v_and_or_b32 v128, v130, s85, v86
	v_and_or_b32 v129, v131, s85, v104
	v_and_or_b32 v130, v132, s85, v105
	v_and_or_b32 v131, v133, s85, v106
	v_and_or_b32 v132, v134, s85, v87
	v_and_or_b32 v133, v135, s85, v107
	v_and_or_b32 v134, v136, s85, v108
	v_and_or_b32 v135, v137, s85, v109
	v_and_or_b32 v68, v68, s85, v88
	v_and_or_b32 v69, v69, s85, v110
	v_and_or_b32 v70, v70, s85, v111
	v_and_or_b32 v71, v71, s85, v112
	v_max_u32_e32 v136, v64, v65
	v_min_u32_e32 v64, v64, v65
	v_max_u32_e32 v65, v67, v66
	v_min_u32_e32 v66, v67, v66
	v_max_u32_e32 v67, v72, v73
	v_min_u32_e32 v72, v72, v73
	v_max_u32_e32 v73, v115, v114
	v_min_u32_e32 v114, v115, v114
	v_max_u32_e32 v115, v116, v117
	v_min_u32_e32 v116, v116, v117
	v_max_u32_e32 v117, v119, v118
	v_min_u32_e32 v118, v119, v118
	v_max_u32_e32 v119, v120, v121
	v_min_u32_e32 v120, v120, v121
	v_max_u32_e32 v121, v123, v122
	v_min_u32_e32 v122, v123, v122
	v_max_u32_e32 v144, v124, v125
	v_min_u32_e32 v124, v124, v125
	v_max_u32_e32 v125, v127, v126
	v_min_u32_e32 v126, v127, v126
	v_max_u32_e32 v127, v128, v129
	v_min_u32_e32 v128, v128, v129
	v_max_u32_e32 v129, v131, v130
	v_min_u32_e32 v130, v131, v130
	v_max_u32_e32 v131, v132, v133
	v_min_u32_e32 v132, v132, v133
	v_max_u32_e32 v133, v135, v134
	v_min_u32_e32 v134, v135, v134
	v_max_u32_e32 v135, v68, v69
	v_min_u32_e32 v68, v68, v69
	v_max_u32_e32 v69, v71, v70
	v_min_u32_e32 v70, v71, v70
	v_max_u32_e32 v123, v136, v66
	v_min_u32_e32 v66, v136, v66
	v_max_u32_e32 v136, v64, v65
	v_min_u32_e32 v64, v64, v65
	v_max_u32_e32 v65, v114, v67
	v_min_u32_e32 v67, v114, v67
	v_max_u32_e32 v114, v73, v72
	v_min_u32_e32 v72, v73, v72
	v_max_u32_e32 v73, v115, v118
	v_min_u32_e32 v115, v115, v118
	v_max_u32_e32 v118, v116, v117
	v_min_u32_e32 v116, v116, v117
	v_max_u32_e32 v117, v122, v119
	v_min_u32_e32 v119, v122, v119
	v_max_u32_e32 v122, v121, v120
	v_min_u32_e32 v120, v121, v120
	v_max_u32_e32 v71, v144, v126
	v_min_u32_e32 v126, v144, v126
	v_max_u32_e32 v144, v124, v125
	v_min_u32_e32 v124, v124, v125
	v_max_u32_e32 v125, v130, v127
	v_min_u32_e32 v127, v130, v127
	v_max_u32_e32 v130, v129, v128
	v_min_u32_e32 v128, v129, v128
	v_max_u32_e32 v129, v131, v134
	v_min_u32_e32 v131, v131, v134
	v_max_u32_e32 v134, v132, v133
	v_min_u32_e32 v132, v132, v133
	v_max_u32_e32 v133, v70, v135
	v_min_u32_e32 v70, v70, v135
	v_max_u32_e32 v135, v69, v68
	v_min_u32_e32 v68, v69, v68
	v_max_u32_e32 v121, v123, v136
	v_min_u32_e32 v123, v123, v136
	v_max_u32_e32 v136, v66, v64
	v_min_u32_e32 v64, v66, v64
	v_max_u32_e32 v66, v72, v67
	v_min_u32_e32 v67, v72, v67
	v_max_u32_e32 v72, v114, v65
	v_min_u32_e32 v65, v114, v65
	v_max_u32_e32 v114, v73, v118
	v_min_u32_e32 v73, v73, v118
	v_max_u32_e32 v118, v115, v116
	v_min_u32_e32 v115, v115, v116
	v_max_u32_e32 v116, v120, v119
	v_min_u32_e32 v119, v120, v119
	v_max_u32_e32 v120, v122, v117
	v_min_u32_e32 v117, v122, v117
	v_max_u32_e32 v69, v71, v144
	v_min_u32_e32 v71, v71, v144
	v_max_u32_e32 v144, v126, v124
	v_min_u32_e32 v124, v126, v124
	v_max_u32_e32 v126, v128, v127
	v_min_u32_e32 v127, v128, v127
	v_max_u32_e32 v128, v130, v125
	v_min_u32_e32 v125, v130, v125
	v_max_u32_e32 v130, v129, v134
	v_min_u32_e32 v129, v129, v134
	v_max_u32_e32 v134, v131, v132
	v_min_u32_e32 v131, v131, v132
	v_max_u32_e32 v132, v68, v70
	v_min_u32_e32 v68, v68, v70
	v_max_u32_e32 v70, v135, v133
	v_min_u32_e32 v133, v135, v133
	v_max_u32_e32 v122, v121, v67
	v_min_u32_e32 v67, v121, v67
	v_max_u32_e32 v121, v123, v66
	v_min_u32_e32 v66, v123, v66
	v_max_u32_e32 v123, v136, v65
	v_min_u32_e32 v65, v136, v65
	v_max_u32_e32 v136, v64, v72
	v_min_u32_e32 v64, v64, v72
	v_max_u32_e32 v72, v119, v114
	v_min_u32_e32 v114, v119, v114
	v_max_u32_e32 v119, v116, v73
	v_min_u32_e32 v73, v116, v73
	v_max_u32_e32 v116, v117, v118
	v_min_u32_e32 v117, v117, v118
	v_max_u32_e32 v118, v120, v115
	v_min_u32_e32 v115, v120, v115
	v_max_u32_e32 v135, v69, v127
	v_min_u32_e32 v69, v69, v127
	v_max_u32_e32 v127, v71, v126
	v_min_u32_e32 v71, v71, v126
	v_max_u32_e32 v126, v144, v125
	v_min_u32_e32 v125, v144, v125
	v_max_u32_e32 v144, v124, v128
	v_min_u32_e32 v124, v124, v128
	v_max_u32_e32 v128, v68, v130
	v_min_u32_e32 v68, v68, v130
	v_max_u32_e32 v130, v132, v129
	v_min_u32_e32 v129, v132, v129
	v_max_u32_e32 v132, v133, v134
	v_min_u32_e32 v133, v133, v134
	v_max_u32_e32 v134, v70, v131
	v_min_u32_e32 v70, v70, v131
	v_max_u32_e32 v120, v122, v123
	v_min_u32_e32 v122, v122, v123
	v_max_u32_e32 v123, v121, v136
	v_min_u32_e32 v121, v121, v136
	v_max_u32_e32 v136, v67, v65
	v_min_u32_e32 v65, v67, v65
	v_max_u32_e32 v67, v66, v64
	v_min_u32_e32 v64, v66, v64
	v_max_u32_e32 v66, v117, v114
	v_min_u32_e32 v114, v117, v114
	v_max_u32_e32 v117, v115, v73
	v_min_u32_e32 v73, v115, v73
	v_max_u32_e32 v115, v116, v72
	v_min_u32_e32 v72, v116, v72
	v_max_u32_e32 v116, v118, v119
	v_min_u32_e32 v118, v118, v119
	v_max_u32_e32 v131, v135, v126
	v_min_u32_e32 v126, v135, v126
	v_max_u32_e32 v135, v127, v144
	v_min_u32_e32 v127, v127, v144
	v_max_u32_e32 v144, v69, v125
	v_min_u32_e32 v69, v69, v125
	v_max_u32_e32 v125, v71, v124
	v_min_u32_e32 v71, v71, v124
	v_max_u32_e32 v124, v133, v68
	v_min_u32_e32 v68, v133, v68
	v_max_u32_e32 v133, v70, v129
	v_min_u32_e32 v70, v70, v129
	v_max_u32_e32 v129, v132, v128
	v_min_u32_e32 v128, v132, v128
; #define CE_DESC(a, b) do { const unsigned _h = max((a), (b)), _l = min((a), (b)); (a) = _h; (b) = _l; } while (0)
; template <int OFF> __device__ __forceinline__ void bitonic_sort16(unsigned (&x)[32]) {
; #pragma unroll
;     for (int k = 2; k <= 16; k <<= 1)
; #pragma unroll
;         for (int j = k >> 1; j >= 1; j >>= 1)
; #pragma unroll
;             for (int i = 0; i < 16; ++i) { const int l = i ^ j; if (l > i) { if ((i & k) == 0 || k == 16) CE_DESC(x[OFF + i], x[OFF + l]); else CE_DESC(x[OFF + l], x[OFF + i]); } }
; __device__ __forceinline__ void peer_unit(Frame& F, const Args& a, int layer, int unit, bool last) {
;     ...
;             bitonic_sort16<0>(t); bitonic_sort16<16>(t);
; #pragma unroll
;             for (int j = 0; j < 16; ++j) t[j] = max(t[j], t[31 - j]);
;             bitonic_merge16<0>(t);
	v_max_u32_e32 v132, v134, v130
	v_min_u32_e32 v130, v134, v130
	v_max_u32_e32 v119, v120, v123
	v_min_u32_e32 v120, v120, v123
	v_max_u32_e32 v123, v122, v121
	v_min_u32_e32 v121, v122, v121
	v_max_u32_e32 v122, v136, v67
	v_min_u32_e32 v67, v136, v67
	v_max_u32_e32 v136, v65, v64
	v_min_u32_e32 v64, v65, v64
	v_max_u32_e32 v65, v73, v114
	v_min_u32_e32 v73, v73, v114
	v_max_u32_e32 v114, v117, v66
	v_min_u32_e32 v66, v117, v66
	v_max_u32_e32 v117, v118, v72
	v_min_u32_e32 v72, v118, v72
	v_max_u32_e32 v118, v116, v115
	v_min_u32_e32 v115, v116, v115
	v_max_u32_e32 v134, v131, v135
	v_min_u32_e32 v131, v131, v135
	v_max_u32_e32 v135, v126, v127
	v_min_u32_e32 v126, v126, v127
	v_max_u32_e32 v127, v144, v125
	v_min_u32_e32 v125, v144, v125
	v_max_u32_e32 v144, v69, v71
	v_min_u32_e32 v69, v69, v71
	v_max_u32_e32 v71, v70, v68
	v_min_u32_e32 v68, v70, v68
	v_max_u32_e32 v70, v133, v124
	v_min_u32_e32 v124, v133, v124
	v_max_u32_e32 v133, v130, v128
	v_min_u32_e32 v128, v130, v128
	v_max_u32_e32 v130, v132, v129
	v_min_u32_e32 v129, v132, v129
	v_max_u32_e32 v116, v119, v73
	v_min_u32_e32 v73, v119, v73
	v_max_u32_e32 v119, v120, v65
	v_min_u32_e32 v65, v120, v65
	v_max_u32_e32 v120, v123, v66
	v_min_u32_e32 v66, v123, v66
	v_max_u32_e32 v123, v121, v114
	v_min_u32_e32 v114, v121, v114
	v_max_u32_e32 v121, v122, v72
	v_min_u32_e32 v72, v122, v72
	v_max_u32_e32 v122, v67, v117
	v_min_u32_e32 v67, v67, v117
	v_max_u32_e32 v117, v136, v115
	v_min_u32_e32 v115, v136, v115
	v_max_u32_e32 v136, v64, v118
	v_min_u32_e32 v64, v64, v118
	v_max_u32_e32 v132, v134, v68
	v_min_u32_e32 v68, v134, v68
	v_max_u32_e32 v134, v131, v71
	v_min_u32_e32 v71, v131, v71
	v_max_u32_e32 v131, v135, v124
	v_min_u32_e32 v124, v135, v124
	v_max_u32_e32 v135, v126, v70
	v_min_u32_e32 v70, v126, v70
	v_max_u32_e32 v126, v127, v128
	v_min_u32_e32 v127, v127, v128
	v_max_u32_e32 v128, v125, v133
	v_min_u32_e32 v125, v125, v133
	v_max_u32_e32 v133, v144, v129
	v_min_u32_e32 v129, v144, v129
	v_max_u32_e32 v144, v69, v130
	v_min_u32_e32 v69, v69, v130
	v_max_u32_e32 v118, v116, v121
	v_min_u32_e32 v116, v116, v121
	v_max_u32_e32 v121, v119, v122
	v_min_u32_e32 v119, v119, v122
	v_max_u32_e32 v122, v120, v117
	v_min_u32_e32 v117, v120, v117
	v_max_u32_e32 v120, v123, v136
	v_min_u32_e32 v123, v123, v136
	v_max_u32_e32 v136, v73, v72
	v_min_u32_e32 v72, v73, v72
	v_max_u32_e32 v73, v65, v67
	v_min_u32_e32 v65, v65, v67
	v_max_u32_e32 v67, v66, v115
	v_min_u32_e32 v66, v66, v115
	v_max_u32_e32 v115, v114, v64
	v_min_u32_e32 v64, v114, v64
	v_max_u32_e32 v130, v132, v126
	v_min_u32_e32 v126, v132, v126
	v_max_u32_e32 v132, v134, v128
	v_min_u32_e32 v128, v134, v128
	v_max_u32_e32 v134, v131, v133
	v_min_u32_e32 v131, v131, v133
	v_max_u32_e32 v133, v135, v144
	v_min_u32_e32 v135, v135, v144
	v_max_u32_e32 v144, v68, v127
	v_min_u32_e32 v68, v68, v127
	v_max_u32_e32 v127, v71, v125
	v_min_u32_e32 v71, v71, v125
	v_max_u32_e32 v125, v124, v129
	v_min_u32_e32 v124, v124, v129
	v_max_u32_e32 v129, v70, v69
	v_min_u32_e32 v69, v70, v69
	v_max_u32_e32 v114, v118, v122
	v_min_u32_e32 v118, v118, v122
	v_max_u32_e32 v122, v121, v120
	v_min_u32_e32 v120, v121, v120
	v_max_u32_e32 v121, v116, v117
	v_min_u32_e32 v116, v116, v117
	v_max_u32_e32 v117, v119, v123
	v_min_u32_e32 v119, v119, v123
	v_max_u32_e32 v123, v136, v67
	v_min_u32_e32 v67, v136, v67
	v_max_u32_e32 v136, v73, v115
	v_min_u32_e32 v73, v73, v115
	v_max_u32_e32 v115, v72, v66
	v_min_u32_e32 v66, v72, v66
	v_max_u32_e32 v72, v65, v64
	v_min_u32_e32 v64, v65, v64
	v_max_u32_e32 v70, v130, v134
	v_min_u32_e32 v130, v130, v134
	v_max_u32_e32 v134, v132, v133
	v_min_u32_e32 v132, v132, v133
	v_max_u32_e32 v133, v126, v131
	v_min_u32_e32 v126, v126, v131
	v_max_u32_e32 v131, v128, v135
	v_min_u32_e32 v128, v128, v135
	v_max_u32_e32 v135, v144, v125
	v_min_u32_e32 v125, v144, v125
	v_max_u32_e32 v144, v127, v129
	v_min_u32_e32 v127, v127, v129
	v_max_u32_e32 v129, v68, v124
	v_min_u32_e32 v68, v68, v124
	v_max_u32_e32 v124, v71, v69
	v_min_u32_e32 v69, v71, v69
	v_min_u32_e32 v65, v114, v122
	v_min_u32_e32 v137, v118, v120
	v_min_u32_e32 v138, v121, v117
	v_min_u32_e32 v139, v116, v119
	v_min_u32_e32 v140, v123, v136
	v_min_u32_e32 v141, v67, v73
	v_min_u32_e32 v142, v115, v72
	v_min_u32_e32 v143, v66, v64
	v_min_u32_e32 v71, v70, v134
	v_min_u32_e32 v145, v130, v132
	v_min_u32_e32 v146, v133, v131
	v_min_u32_e32 v147, v126, v128
	v_min_u32_e32 v148, v135, v144
	v_min_u32_e32 v149, v125, v127
	v_min_u32_e32 v151, v129, v124
	v_min_u32_e32 v152, v68, v69
	v_max3_u32 v114, v114, v122, v152
	v_max3_u32 v65, v65, v68, v69
	v_max3_u32 v68, v118, v120, v151
	v_max3_u32 v69, v137, v129, v124
	v_max3_u32 v117, v121, v117, v149
	v_max3_u32 v118, v138, v125, v127
	v_max3_u32 v116, v116, v119, v148
	v_max3_u32 v119, v139, v135, v144
	v_max3_u32 v120, v123, v136, v147
	v_max3_u32 v121, v140, v126, v128
	v_max3_u32 v67, v67, v73, v146
	v_max3_u32 v73, v141, v133, v131
	v_max3_u32 v72, v115, v72, v145
	v_max3_u32 v115, v142, v130, v132
	v_max3_u32 v64, v66, v64, v71
	v_max3_u32 v66, v143, v70, v134
	v_max_u32_e32 v70, v114, v120
	v_min_u32_e32 v71, v114, v120
	v_max_u32_e32 v114, v65, v121
	v_max_u32_e32 v120, v68, v67
	v_min_u32_e32 v67, v68, v67
	v_max_u32_e32 v68, v69, v73
	v_min_u32_e32 v69, v69, v73
	v_max_u32_e32 v73, v117, v72
	v_min_u32_e32 v72, v117, v72
	v_max_u32_e32 v117, v118, v115
	v_min_u32_e32 v115, v118, v115
	v_max_u32_e32 v118, v116, v64
	v_min_u32_e32 v64, v116, v64
	v_max_u32_e32 v116, v119, v66
	v_min_u32_e32 v65, v65, v121
	v_min_u32_e32 v66, v119, v66
	v_max_u32_e32 v119, v70, v73
	v_min_u32_e32 v70, v70, v73
; __device__ __forceinline__ unsigned xor16_u(unsigned x, int lane) { const auto r = __builtin_amdgcn_permlane16_swap(x, x, false, false); return (lane & 16) ? (unsigned)r[0] : (unsigned)r[1]; }
; __device__ __forceinline__ unsigned xor32_u(unsigned x, int lane) { const auto r = __builtin_amdgcn_permlane32_swap(x, x, false, false); return (lane & 32) ? (unsigned)r[0] : (unsigned)r[1]; }
; __device__ __forceinline__ void peer_unit(Frame& F, const Args& a, int layer, int unit, bool last) {
;     ...
;             bitonic_merge16<0>(t);
; #pragma unroll
;             for (int rnd = 0; rnd < 2; ++rnd) {
; #pragma unroll
;                 for (int j = 0; j < 16; ++j) t[16 + j] = rnd ? xor32_u(t[j], lane) : xor16_u(t[j], lane);
; #pragma unroll
;                 for (int j = 0; j < 16; ++j) t[j] = max(t[j], t[31 - j]);
;                 bitonic_merge16<0>(t); }
	v_max_u32_e32 v73, v114, v117
	v_min_u32_e32 v114, v114, v117
	v_max_u32_e32 v117, v120, v118
	v_min_u32_e32 v118, v120, v118
	v_max_u32_e32 v120, v68, v116
	v_min_u32_e32 v68, v68, v116
	v_max_u32_e32 v116, v71, v72
	v_min_u32_e32 v71, v71, v72
	v_max_u32_e32 v72, v65, v115
	v_min_u32_e32 v65, v65, v115
	v_max_u32_e32 v115, v67, v64
	v_min_u32_e32 v64, v67, v64
	v_max_u32_e32 v67, v69, v66
	v_min_u32_e32 v66, v69, v66
	v_max_u32_e32 v69, v119, v117
	v_min_u32_e32 v117, v119, v117
	v_max_u32_e32 v119, v73, v120
	v_min_u32_e32 v73, v73, v120
	v_max_u32_e32 v120, v70, v118
	v_min_u32_e32 v70, v70, v118
	v_max_u32_e32 v118, v114, v68
	v_min_u32_e32 v68, v114, v68
	v_max_u32_e32 v114, v116, v115
	v_min_u32_e32 v115, v116, v115
	v_max_u32_e32 v116, v72, v67
	v_min_u32_e32 v67, v72, v67
	v_max_u32_e32 v72, v71, v64
	v_min_u32_e32 v64, v71, v64
	v_max_u32_e32 v71, v65, v66
	v_min_u32_e32 v65, v65, v66
	v_max_u32_e32 v66, v69, v119
	v_min_u32_e32 v69, v69, v119
	v_max_u32_e32 v119, v117, v73
	v_min_u32_e32 v73, v117, v73
	v_max_u32_e32 v117, v120, v118
	v_min_u32_e32 v118, v120, v118
	v_max_u32_e32 v120, v70, v68
	v_min_u32_e32 v68, v70, v68
	v_max_u32_e32 v70, v114, v116
	v_min_u32_e32 v114, v114, v116
	v_max_u32_e32 v116, v115, v67
	v_min_u32_e32 v67, v115, v67
	v_max_u32_e32 v115, v72, v71
	v_min_u32_e32 v71, v72, v71
	v_max_u32_e32 v72, v64, v65
	v_min_u32_e32 v64, v64, v65
	v_mov_b32_e32 v65, v66
	v_mov_b32_e32 v121, v66
	s_nop 1
	v_permlane16_swap_b32_e32 v65, v121
	v_cndmask_b32_e64 v65, v65, v121, s[40:41]
	v_mov_b32_e32 v121, v69
	v_mov_b32_e32 v122, v69
	s_nop 1
	v_permlane16_swap_b32_e32 v121, v122
	v_cndmask_b32_e64 v121, v121, v122, s[40:41]
	v_mov_b32_e32 v122, v119
	v_mov_b32_e32 v123, v119
	s_nop 1
	v_permlane16_swap_b32_e32 v122, v123
	v_cndmask_b32_e64 v122, v122, v123, s[40:41]
	v_mov_b32_e32 v123, v73
	v_mov_b32_e32 v124, v73
	s_nop 1
	v_permlane16_swap_b32_e32 v123, v124
	v_cndmask_b32_e64 v123, v123, v124, s[40:41]
	v_mov_b32_e32 v124, v117
	v_mov_b32_e32 v125, v117
	s_nop 1
	v_permlane16_swap_b32_e32 v124, v125
	v_cndmask_b32_e64 v124, v124, v125, s[40:41]
	v_mov_b32_e32 v125, v118
	v_mov_b32_e32 v126, v118
	s_nop 1
	v_permlane16_swap_b32_e32 v125, v126
	v_cndmask_b32_e64 v125, v125, v126, s[40:41]
	v_mov_b32_e32 v126, v120
	v_mov_b32_e32 v127, v120
	s_nop 1
	v_permlane16_swap_b32_e32 v126, v127
	v_cndmask_b32_e64 v126, v126, v127, s[40:41]
	v_mov_b32_e32 v127, v68
	v_mov_b32_e32 v128, v68
	s_nop 1
	v_permlane16_swap_b32_e32 v127, v128
	v_cndmask_b32_e64 v127, v127, v128, s[40:41]
	v_mov_b32_e32 v128, v70
	v_mov_b32_e32 v129, v70
	s_nop 1
	v_permlane16_swap_b32_e32 v128, v129
	v_cndmask_b32_e64 v128, v128, v129, s[40:41]
	v_mov_b32_e32 v129, v114
	v_mov_b32_e32 v130, v114
	s_nop 1
	v_permlane16_swap_b32_e32 v129, v130
	v_cndmask_b32_e64 v129, v129, v130, s[40:41]
	v_mov_b32_e32 v130, v116
	v_mov_b32_e32 v131, v116
	s_nop 1
	v_permlane16_swap_b32_e32 v130, v131
	v_cndmask_b32_e64 v130, v130, v131, s[40:41]
	v_mov_b32_e32 v131, v67
	v_mov_b32_e32 v132, v67
	s_nop 1
	v_permlane16_swap_b32_e32 v131, v132
	v_cndmask_b32_e64 v131, v131, v132, s[40:41]
	v_mov_b32_e32 v132, v115
	v_mov_b32_e32 v133, v115
	s_nop 1
	v_permlane16_swap_b32_e32 v132, v133
	v_cndmask_b32_e64 v132, v132, v133, s[40:41]
	v_mov_b32_e32 v133, v71
	v_mov_b32_e32 v134, v71
	s_nop 1
	v_permlane16_swap_b32_e32 v133, v134
	v_cndmask_b32_e64 v133, v133, v134, s[40:41]
	v_mov_b32_e32 v134, v72
	v_mov_b32_e32 v135, v72
	s_nop 1
	v_permlane16_swap_b32_e32 v134, v135
	v_cndmask_b32_e64 v134, v134, v135, s[40:41]
	v_mov_b32_e32 v135, v64
	v_mov_b32_e32 v136, v64
	s_nop 1
	v_permlane16_swap_b32_e32 v135, v136
	v_cndmask_b32_e64 v135, v135, v136, s[40:41]
	v_max_u32_e32 v66, v66, v135
	v_max_u32_e32 v69, v69, v134
	v_max_u32_e32 v119, v119, v133
	v_max_u32_e32 v73, v73, v132
	v_max_u32_e32 v117, v117, v131
	v_max_u32_e32 v118, v118, v130
	v_max_u32_e32 v120, v120, v129
	v_max_u32_e32 v68, v68, v128
	v_max_u32_e32 v70, v70, v127
	v_max_u32_e32 v114, v114, v126
	v_max_u32_e32 v116, v116, v125
	v_max_u32_e32 v67, v67, v124
	v_max_u32_e32 v115, v115, v123
	v_max_u32_e32 v71, v71, v122
	v_max_u32_e32 v72, v72, v121
	v_max_u32_e32 v64, v64, v65
	v_max_u32_e32 v65, v66, v70
	v_min_u32_e32 v66, v66, v70
	v_max_u32_e32 v70, v69, v114
	v_min_u32_e32 v69, v69, v114
	v_max_u32_e32 v114, v119, v116
	v_min_u32_e32 v116, v119, v116
	v_max_u32_e32 v119, v73, v67
	v_min_u32_e32 v67, v73, v67
	v_max_u32_e32 v73, v117, v115
	v_min_u32_e32 v115, v117, v115
	v_max_u32_e32 v117, v118, v71
	v_min_u32_e32 v71, v118, v71
	v_max_u32_e32 v118, v120, v72
	v_min_u32_e32 v72, v120, v72
	v_max_u32_e32 v120, v68, v64
	v_min_u32_e32 v64, v68, v64
	v_max_u32_e32 v68, v65, v73
	v_min_u32_e32 v65, v65, v73
	v_max_u32_e32 v73, v70, v117
	v_min_u32_e32 v70, v70, v117
	v_max_u32_e32 v117, v114, v118
	v_min_u32_e32 v114, v114, v118
	v_max_u32_e32 v118, v119, v120
	v_min_u32_e32 v119, v119, v120
	v_max_u32_e32 v120, v66, v115
	v_min_u32_e32 v66, v66, v115
	v_max_u32_e32 v115, v69, v71
	v_min_u32_e32 v69, v69, v71
	v_max_u32_e32 v71, v116, v72
	v_min_u32_e32 v72, v116, v72
	v_max_u32_e32 v116, v67, v64
	v_min_u32_e32 v64, v67, v64
	v_max_u32_e32 v67, v68, v117
	v_min_u32_e32 v68, v68, v117
	v_max_u32_e32 v117, v73, v118
	v_min_u32_e32 v73, v73, v118
	v_max_u32_e32 v118, v65, v114
	v_min_u32_e32 v65, v65, v114
	v_max_u32_e32 v114, v70, v119
	v_min_u32_e32 v70, v70, v119
	v_max_u32_e32 v119, v120, v71
	v_min_u32_e32 v71, v120, v71
	v_max_u32_e32 v120, v115, v116
	v_min_u32_e32 v115, v115, v116
	v_max_u32_e32 v116, v66, v72
	v_min_u32_e32 v66, v66, v72
	v_max_u32_e32 v72, v69, v64
	v_min_u32_e32 v64, v69, v64
; __device__ __forceinline__ unsigned xor16_u(unsigned x, int lane) { const auto r = __builtin_amdgcn_permlane16_swap(x, x, false, false); return (lane & 16) ? (unsigned)r[0] : (unsigned)r[1]; }
; __device__ __forceinline__ unsigned xor32_u(unsigned x, int lane) { const auto r = __builtin_amdgcn_permlane32_swap(x, x, false, false); return (lane & 32) ? (unsigned)r[0] : (unsigned)r[1]; }
; #define K_STORE(J) do { _Pragma("unroll") for (int _i = 0; _i < 4; ++_i) { const int _pc = tid + 512 * _i, _rr = _pc >> 4, _c16 = _pc & 15; *(LAS v4u*)(sKey + ((J) & 1) * 128 * TP + _rr * TP + _c16 * 8) = ktn[_i]; } } while (0)
; __device__ __forceinline__ void peer_unit(Frame& F, const Args& a, int layer, int unit, bool last) {
;     ...
;             for (int rnd = 0; rnd < 2; ++rnd) {
; #pragma unroll
;                 for (int j = 0; j < 16; ++j) t[16 + j] = rnd ? xor32_u(t[j], lane) : xor16_u(t[j], lane);
; #pragma unroll
;                 for (int j = 0; j < 16; ++j) t[j] = max(t[j], t[31 - j]);
;                 bitonic_merge16<0>(t); }
; #pragma unroll
;             for (int j = 0; j < 16; ++j) sLT[fr * 32 + p * 16 + j] = t[j];
;             if (jp + 1 < 16) { K_STORE(jp + 1);
; #pragma unroll
;                 for (int kk = 0; kk < 4; ++kk) qf[kk] = qfn[kk]; }
	v_max_u32_e32 v69, v67, v117
	v_min_u32_e32 v67, v67, v117
	v_max_u32_e32 v117, v68, v73
	v_min_u32_e32 v68, v68, v73
	v_max_u32_e32 v73, v118, v114
	v_min_u32_e32 v114, v118, v114
	v_max_u32_e32 v118, v65, v70
	v_min_u32_e32 v65, v65, v70
	v_max_u32_e32 v70, v119, v120
	v_min_u32_e32 v119, v119, v120
	v_max_u32_e32 v120, v71, v115
	v_min_u32_e32 v71, v71, v115
	v_max_u32_e32 v115, v116, v72
	v_min_u32_e32 v72, v116, v72
	v_max_u32_e32 v116, v66, v64
	v_min_u32_e32 v64, v66, v64
	v_mov_b32_e32 v66, v69
	v_mov_b32_e32 v121, v69
	s_nop 1
	v_permlane32_swap_b32_e32 v66, v121
	v_cndmask_b32_e64 v66, v66, v121, s[38:39]
	v_mov_b32_e32 v121, v67
	v_mov_b32_e32 v122, v67
	s_nop 1
	v_permlane32_swap_b32_e32 v121, v122
	v_cndmask_b32_e64 v121, v121, v122, s[38:39]
	v_mov_b32_e32 v122, v117
	v_mov_b32_e32 v123, v117
	s_nop 1
	v_permlane32_swap_b32_e32 v122, v123
	v_cndmask_b32_e64 v122, v122, v123, s[38:39]
	v_mov_b32_e32 v123, v68
	v_mov_b32_e32 v124, v68
	s_nop 1
	v_permlane32_swap_b32_e32 v123, v124
	v_cndmask_b32_e64 v123, v123, v124, s[38:39]
	v_mov_b32_e32 v124, v73
	v_mov_b32_e32 v125, v73
	s_nop 1
	v_permlane32_swap_b32_e32 v124, v125
	v_cndmask_b32_e64 v124, v124, v125, s[38:39]
	v_mov_b32_e32 v125, v114
	v_mov_b32_e32 v126, v114
	s_nop 1
	v_permlane32_swap_b32_e32 v125, v126
	v_cndmask_b32_e64 v125, v125, v126, s[38:39]
	v_mov_b32_e32 v126, v118
	v_mov_b32_e32 v127, v118
	s_nop 1
	v_permlane32_swap_b32_e32 v126, v127
	v_cndmask_b32_e64 v126, v126, v127, s[38:39]
	v_mov_b32_e32 v127, v65
	v_mov_b32_e32 v128, v65
	s_nop 1
	v_permlane32_swap_b32_e32 v127, v128
	v_cndmask_b32_e64 v127, v127, v128, s[38:39]
	v_mov_b32_e32 v128, v70
	v_mov_b32_e32 v129, v70
	s_nop 1
	v_permlane32_swap_b32_e32 v128, v129
	v_cndmask_b32_e64 v128, v128, v129, s[38:39]
	v_mov_b32_e32 v129, v119
	v_mov_b32_e32 v130, v119
	s_nop 1
	v_permlane32_swap_b32_e32 v129, v130
	v_cndmask_b32_e64 v129, v129, v130, s[38:39]
	v_mov_b32_e32 v130, v120
	v_mov_b32_e32 v131, v120
	s_nop 1
	v_permlane32_swap_b32_e32 v130, v131
	v_cndmask_b32_e64 v130, v130, v131, s[38:39]
	v_mov_b32_e32 v131, v71
	v_mov_b32_e32 v132, v71
	s_nop 1
	v_permlane32_swap_b32_e32 v131, v132
	v_cndmask_b32_e64 v131, v131, v132, s[38:39]
	v_mov_b32_e32 v132, v115
	v_mov_b32_e32 v133, v115
	s_nop 1
	v_permlane32_swap_b32_e32 v132, v133
	v_cndmask_b32_e64 v132, v132, v133, s[38:39]
	v_mov_b32_e32 v133, v72
	v_mov_b32_e32 v134, v72
	s_nop 1
	v_permlane32_swap_b32_e32 v133, v134
	v_cndmask_b32_e64 v133, v133, v134, s[38:39]
	v_mov_b32_e32 v134, v116
	v_mov_b32_e32 v135, v116
	s_nop 1
	v_permlane32_swap_b32_e32 v134, v135
	v_cndmask_b32_e64 v134, v134, v135, s[38:39]
	v_mov_b32_e32 v135, v64
	v_mov_b32_e32 v136, v64
	s_nop 1
	v_permlane32_swap_b32_e32 v135, v136
	v_cndmask_b32_e64 v135, v135, v136, s[38:39]
	v_max_u32_e32 v69, v69, v135
	v_max_u32_e32 v67, v67, v134
	v_max_u32_e32 v117, v117, v133
	v_max_u32_e32 v68, v68, v132
	v_max_u32_e32 v73, v73, v131
	v_max_u32_e32 v114, v114, v130
	v_max_u32_e32 v118, v118, v129
	v_max_u32_e32 v65, v65, v128
	v_max_u32_e32 v70, v70, v127
	v_max_u32_e32 v119, v119, v126
	v_max_u32_e32 v120, v120, v125
	v_max_u32_e32 v71, v71, v124
	v_max_u32_e32 v115, v115, v123
	v_max_u32_e32 v72, v72, v122
	v_max_u32_e32 v116, v116, v121
	v_max_u32_e32 v64, v64, v66
	v_max_u32_e32 v66, v69, v70
	v_min_u32_e32 v69, v69, v70
	v_max_u32_e32 v70, v67, v119
	v_min_u32_e32 v67, v67, v119
	v_max_u32_e32 v119, v117, v120
	v_min_u32_e32 v117, v117, v120
	v_max_u32_e32 v120, v68, v71
	v_min_u32_e32 v68, v68, v71
	v_max_u32_e32 v71, v73, v115
	v_min_u32_e32 v73, v73, v115
	v_max_u32_e32 v115, v114, v72
	v_min_u32_e32 v72, v114, v72
	v_max_u32_e32 v114, v118, v116
	v_min_u32_e32 v116, v118, v116
	v_max_u32_e32 v118, v65, v64
	v_min_u32_e32 v64, v65, v64
	v_max_u32_e32 v65, v66, v71
	v_min_u32_e32 v66, v66, v71
	v_max_u32_e32 v71, v70, v115
	v_min_u32_e32 v70, v70, v115
	v_max_u32_e32 v115, v119, v114
	v_min_u32_e32 v114, v119, v114
	v_max_u32_e32 v119, v120, v118
	v_min_u32_e32 v118, v120, v118
	v_max_u32_e32 v120, v69, v73
	v_min_u32_e32 v69, v69, v73
	v_max_u32_e32 v73, v67, v72
	v_min_u32_e32 v67, v67, v72
	v_max_u32_e32 v72, v117, v116
	v_min_u32_e32 v116, v117, v116
	v_max_u32_e32 v117, v68, v64
	v_min_u32_e32 v64, v68, v64
	v_max_u32_e32 v68, v65, v115
	v_min_u32_e32 v115, v65, v115
	v_max_u32_e32 v65, v71, v119
	v_min_u32_e32 v71, v71, v119
	v_max_u32_e32 v122, v120, v72
	v_min_u32_e32 v72, v120, v72
	v_max_u32_e32 v120, v73, v117
	v_min_u32_e32 v73, v73, v117
	v_max_u32_e32 v119, v66, v114
	v_min_u32_e32 v114, v66, v114
	v_max_u32_e32 v121, v70, v118
	v_min_u32_e32 v118, v70, v118
	v_max_u32_e32 v123, v69, v116
	v_min_u32_e32 v124, v69, v116
	v_max_u32_e32 v125, v67, v64
	v_min_u32_e32 v126, v67, v64
	v_max_u32_e32 v64, v68, v65
	v_min_u32_e32 v65, v68, v65
	v_max_u32_e32 v66, v115, v71
	v_min_u32_e32 v67, v115, v71
	v_max_u32_e32 v116, v72, v73
	v_min_u32_e32 v117, v72, v73
	v_lshl_add_u32 v72, s55, 6, v75
	v_max_u32_e32 v68, v119, v121
	v_min_u32_e32 v69, v119, v121
	v_max_u32_e32 v70, v114, v118
	v_min_u32_e32 v71, v114, v118
	v_max_u32_e32 v114, v122, v120
	v_min_u32_e32 v115, v122, v120
	v_max_u32_e32 v118, v123, v125
	v_min_u32_e32 v119, v123, v125
	v_max_u32_e32 v120, v124, v126
	v_min_u32_e32 v121, v124, v126
	ds_write_b128 v72, v[64:67]
	ds_write_b128 v72, v[68:71] offset:16
	ds_write_b128 v72, v[114:117] offset:32
	ds_write_b128 v72, v[118:121] offset:48
	s_cbranch_vccnz .LBB0_1706
	s_lshl_b32 s5, s54, 7
	s_and_b32 s5, s5, 0x80
	s_mulk_i32 s5, 0x110
	v_add_u32_e32 v18, s5, v78
	v_add_u32_e32 v19, v18, v81
	v_add_u32_e32 v20, v18, v80
	v_add_u32_e32 v21, v18, v79
	v_add_u32_e32 v18, v18, v77
	s_waitcnt vmcnt(7)
	ds_write_b128 v18, v[2:5]
	s_waitcnt vmcnt(6)
	ds_write_b128 v21, v[6:9]
	s_waitcnt vmcnt(5)
	ds_write_b128 v20, v[10:13]
	s_waitcnt vmcnt(4)
	ds_write_b128 v19, v[14:17]
	s_waitcnt vmcnt(3)
	v_mov_b64_e32 v[18:19], v[34:35]
	s_waitcnt vmcnt(2)
	v_mov_b64_e32 v[22:23], v[38:39]
	s_waitcnt vmcnt(1)
	v_mov_b64_e32 v[26:27], v[42:43]
	s_waitcnt vmcnt(0)
	v_mov_b64_e32 v[30:31], v[46:47]
	v_mov_b64_e32 v[20:21], v[36:37]
	v_mov_b64_e32 v[24:25], v[40:41]
	v_mov_b64_e32 v[28:29], v[44:45]
	v_mov_b64_e32 v[32:33], v[48:49]
	s_branch .LBB0_1706
